# adds batched LRU chunk carry-in loads (34 aggregate loads issued at once instead of serialized load-wait pairs) on top of attention read pipelining
# speedup vs baseline: 1.0197x; 1.0021x over previous
; __device__ __forceinline__ void ph_lru(const Ptrs& P, unsigned char* lds, int mode, int item0) {
;     ...
;         if (mode == 1 && wid < 2) {
;             const int dir = wid, pos = dir == 0 ? c : bwd_pos(c); float h = 0.f;
;             for (int p0 = 0; p0 < pos; p0 += 8) {
;                 float2 ag[8];
; #pragma unroll
;                 for (int i = 0; i < 8; ++i) { const int p = p0 + i, pc = p < pos ? p : p0, cc = dir == 0 ? pc : bwd_chunk_at(pc);
;                     ag[i] = *(const float2*)(agg + ((((size_t)b * NCH + cc) * 2 + dir) * 512 + n * 64 + lane) * 2); if (p >= pos) { ag[i].x = 1.f; ag[i].y = 0.f; } }
; #pragma unroll
;                 for (int i = 0; i < 8; ++i) h = ag[i].x * h + ag[i].y;
;             }
;             CAR[dir * 64 + lane] = h;
.LBB0_1103:
	s_mul_hi_i32 s0, s44, 0x78787879
	s_lshr_b32 s1, s0, 31
	s_ashr_i32 s61, s0, 7
	s_add_i32 s61, s61, s1
	s_and_saveexec_b64 s[0:1], s[4:5]
	s_cbranch_execz .LBB0_1111
	s_cmp_gt_i32 s38, 1
	s_cselect_b32 s33, 35, 1
	s_sub_i32 s33, s33, s38
	v_mov_b32_e32 v50, s38
	v_mov_b32_e32 v51, s33
	v_cndmask_b32_e64 v54, v50, v51, s[12:13]
	s_lshl_b32 s52, s30, 6
	s_ashr_i32 s53, s52, 31
	v_lshl_add_u64 v[50:51], s[52:53], 0, v[68:69]
	v_lshlrev_b32_e32 v50, 3, v50
	s_mul_i32 s44, s61, 34
	s_lshl_b32 s44, s44, 13
	s_add_u32 s52, s26, s44
	s_addc_u32 s53, s27, 0
	v_cndmask_b32_e64 v52, 0, 1, s[12:13]
	v_lshl_add_u32 v52, v52, 13, v50
	global_load_dwordx2 v[186:187], v52, s[52:53]
	v_cndmask_b32_e64 v52, 1, 0, s[12:13]
	v_lshl_add_u32 v52, v52, 13, v50
	global_load_dwordx2 v[188:189], v52, s[52:53]
	v_cndmask_b32_e64 v52, 2, 33, s[12:13]
	v_lshl_add_u32 v52, v52, 13, v50
	global_load_dwordx2 v[190:191], v52, s[52:53]
	v_cndmask_b32_e64 v52, 3, 32, s[12:13]
	v_lshl_add_u32 v52, v52, 13, v50
	global_load_dwordx2 v[192:193], v52, s[52:53]
	v_cndmask_b32_e64 v52, 4, 31, s[12:13]
	v_lshl_add_u32 v52, v52, 13, v50
	global_load_dwordx2 v[194:195], v52, s[52:53]
	v_cndmask_b32_e64 v52, 5, 30, s[12:13]
	v_lshl_add_u32 v52, v52, 13, v50
	global_load_dwordx2 v[196:197], v52, s[52:53]
	v_cndmask_b32_e64 v52, 6, 29, s[12:13]
	v_lshl_add_u32 v52, v52, 13, v50
	global_load_dwordx2 v[198:199], v52, s[52:53]
	v_cndmask_b32_e64 v52, 7, 28, s[12:13]
	v_lshl_add_u32 v52, v52, 13, v50
	global_load_dwordx2 v[200:201], v52, s[52:53]
	v_cndmask_b32_e64 v52, 8, 27, s[12:13]
	v_lshl_add_u32 v52, v52, 13, v50
	global_load_dwordx2 v[202:203], v52, s[52:53]
	v_cndmask_b32_e64 v52, 9, 26, s[12:13]
	v_lshl_add_u32 v52, v52, 13, v50
	global_load_dwordx2 v[204:205], v52, s[52:53]
	v_cndmask_b32_e64 v52, 10, 25, s[12:13]
	v_lshl_add_u32 v52, v52, 13, v50
	global_load_dwordx2 v[206:207], v52, s[52:53]
	v_cndmask_b32_e64 v52, 11, 24, s[12:13]
	v_lshl_add_u32 v52, v52, 13, v50
	global_load_dwordx2 v[208:209], v52, s[52:53]
	v_cndmask_b32_e64 v52, 12, 23, s[12:13]
	v_lshl_add_u32 v52, v52, 13, v50
	global_load_dwordx2 v[210:211], v52, s[52:53]
	v_cndmask_b32_e64 v52, 13, 22, s[12:13]
	v_lshl_add_u32 v52, v52, 13, v50
	global_load_dwordx2 v[212:213], v52, s[52:53]
	v_cndmask_b32_e64 v52, 14, 21, s[12:13]
	v_lshl_add_u32 v52, v52, 13, v50
	global_load_dwordx2 v[214:215], v52, s[52:53]
	v_cndmask_b32_e64 v52, 15, 20, s[12:13]
	v_lshl_add_u32 v52, v52, 13, v50
	global_load_dwordx2 v[216:217], v52, s[52:53]
	v_cndmask_b32_e64 v52, 16, 19, s[12:13]
	v_lshl_add_u32 v52, v52, 13, v50
	global_load_dwordx2 v[218:219], v52, s[52:53]
	v_cndmask_b32_e64 v52, 17, 18, s[12:13]
	v_lshl_add_u32 v52, v52, 13, v50
	global_load_dwordx2 v[220:221], v52, s[52:53]
	v_cndmask_b32_e64 v52, 18, 17, s[12:13]
	v_lshl_add_u32 v52, v52, 13, v50
	global_load_dwordx2 v[222:223], v52, s[52:53]
	v_cndmask_b32_e64 v52, 19, 16, s[12:13]
	v_lshl_add_u32 v52, v52, 13, v50
	global_load_dwordx2 v[224:225], v52, s[52:53]
	v_cndmask_b32_e64 v52, 20, 15, s[12:13]
	v_lshl_add_u32 v52, v52, 13, v50
	global_load_dwordx2 v[226:227], v52, s[52:53]
	v_cndmask_b32_e64 v52, 21, 14, s[12:13]
	v_lshl_add_u32 v52, v52, 13, v50
	global_load_dwordx2 v[228:229], v52, s[52:53]
	v_cndmask_b32_e64 v52, 22, 13, s[12:13]
	v_lshl_add_u32 v52, v52, 13, v50
	global_load_dwordx2 v[230:231], v52, s[52:53]
	v_cndmask_b32_e64 v52, 23, 12, s[12:13]
	v_lshl_add_u32 v52, v52, 13, v50
	global_load_dwordx2 v[232:233], v52, s[52:53]
	v_cndmask_b32_e64 v52, 24, 11, s[12:13]
	v_lshl_add_u32 v52, v52, 13, v50
	global_load_dwordx2 v[234:235], v52, s[52:53]
	v_cndmask_b32_e64 v52, 25, 10, s[12:13]
	v_lshl_add_u32 v52, v52, 13, v50
	global_load_dwordx2 v[236:237], v52, s[52:53]
	v_cndmask_b32_e64 v52, 26, 9, s[12:13]
	v_lshl_add_u32 v52, v52, 13, v50
	global_load_dwordx2 v[238:239], v52, s[52:53]
	v_cndmask_b32_e64 v52, 27, 8, s[12:13]
	v_lshl_add_u32 v52, v52, 13, v50
	global_load_dwordx2 v[240:241], v52, s[52:53]
	v_cndmask_b32_e64 v52, 28, 7, s[12:13]
	v_lshl_add_u32 v52, v52, 13, v50
	global_load_dwordx2 v[242:243], v52, s[52:53]
	v_cndmask_b32_e64 v52, 29, 6, s[12:13]
	v_lshl_add_u32 v52, v52, 13, v50
	global_load_dwordx2 v[244:245], v52, s[52:53]
	v_cndmask_b32_e64 v52, 30, 5, s[12:13]
	v_lshl_add_u32 v52, v52, 13, v50
	global_load_dwordx2 v[246:247], v52, s[52:53]
	v_cndmask_b32_e64 v52, 31, 4, s[12:13]
	v_lshl_add_u32 v52, v52, 13, v50
	global_load_dwordx2 v[248:249], v52, s[52:53]
	v_cndmask_b32_e64 v52, 32, 3, s[12:13]
	v_lshl_add_u32 v52, v52, 13, v50
	global_load_dwordx2 v[250:251], v52, s[52:53]
	v_cndmask_b32_e64 v52, 33, 2, s[12:13]
	v_lshl_add_u32 v52, v52, 13, v50
	global_load_dwordx2 v[252:253], v52, s[52:53]
	v_mov_b32_e32 v55, 0
	s_waitcnt vmcnt(33)
	v_cmp_lt_i32_e32 vcc, 0, v54
	s_nop 1
	v_cndmask_b32_e32 v186, 1.0, v186, vcc
	v_cndmask_b32_e32 v187, 0, v187, vcc
	v_fmac_f32_e32 v187, v55, v186
	s_waitcnt vmcnt(32)
	v_cmp_lt_i32_e32 vcc, 1, v54
	s_nop 1
	v_cndmask_b32_e32 v188, 1.0, v188, vcc
	v_cndmask_b32_e32 v189, 0, v189, vcc
	v_fmac_f32_e32 v189, v187, v188
	s_waitcnt vmcnt(31)
	v_cmp_lt_i32_e32 vcc, 2, v54
	s_nop 1
	v_cndmask_b32_e32 v190, 1.0, v190, vcc
	v_cndmask_b32_e32 v191, 0, v191, vcc
	v_fmac_f32_e32 v191, v189, v190
	s_waitcnt vmcnt(30)
; __device__ __forceinline__ void ph_lru(const Ptrs& P, unsigned char* lds, int mode, int item0) {
;     ...
;             for (int p0 = 0; p0 < pos; p0 += 8) {
;                 float2 ag[8];
; #pragma unroll
;                 for (int i = 0; i < 8; ++i) { const int p = p0 + i, pc = p < pos ? p : p0, cc = dir == 0 ? pc : bwd_chunk_at(pc);
;                     ag[i] = *(const float2*)(agg + ((((size_t)b * NCH + cc) * 2 + dir) * 512 + n * 64 + lane) * 2); if (p >= pos) { ag[i].x = 1.f; ag[i].y = 0.f; } }
; #pragma unroll
;                 for (int i = 0; i < 8; ++i) h = ag[i].x * h + ag[i].y;
;             }
;             CAR[dir * 64 + lane] = h;
	v_cmp_lt_i32_e32 vcc, 3, v54
	s_nop 1
	v_cndmask_b32_e32 v192, 1.0, v192, vcc
	v_cndmask_b32_e32 v193, 0, v193, vcc
	v_fmac_f32_e32 v193, v191, v192
	s_waitcnt vmcnt(29)
	v_cmp_lt_i32_e32 vcc, 4, v54
	s_nop 1
	v_cndmask_b32_e32 v194, 1.0, v194, vcc
	v_cndmask_b32_e32 v195, 0, v195, vcc
	v_fmac_f32_e32 v195, v193, v194
	s_waitcnt vmcnt(28)
	v_cmp_lt_i32_e32 vcc, 5, v54
	s_nop 1
	v_cndmask_b32_e32 v196, 1.0, v196, vcc
	v_cndmask_b32_e32 v197, 0, v197, vcc
	v_fmac_f32_e32 v197, v195, v196
	s_waitcnt vmcnt(27)
	v_cmp_lt_i32_e32 vcc, 6, v54
	s_nop 1
	v_cndmask_b32_e32 v198, 1.0, v198, vcc
	v_cndmask_b32_e32 v199, 0, v199, vcc
	v_fmac_f32_e32 v199, v197, v198
	s_waitcnt vmcnt(26)
	v_cmp_lt_i32_e32 vcc, 7, v54
	s_nop 1
	v_cndmask_b32_e32 v200, 1.0, v200, vcc
	v_cndmask_b32_e32 v201, 0, v201, vcc
	v_fmac_f32_e32 v201, v199, v200
	s_waitcnt vmcnt(25)
	v_cmp_lt_i32_e32 vcc, 8, v54
	s_nop 1
	v_cndmask_b32_e32 v202, 1.0, v202, vcc
	v_cndmask_b32_e32 v203, 0, v203, vcc
	v_fmac_f32_e32 v203, v201, v202
	s_waitcnt vmcnt(24)
	v_cmp_lt_i32_e32 vcc, 9, v54
	s_nop 1
	v_cndmask_b32_e32 v204, 1.0, v204, vcc
	v_cndmask_b32_e32 v205, 0, v205, vcc
	v_fmac_f32_e32 v205, v203, v204
	s_waitcnt vmcnt(23)
	v_cmp_lt_i32_e32 vcc, 10, v54
	s_nop 1
	v_cndmask_b32_e32 v206, 1.0, v206, vcc
	v_cndmask_b32_e32 v207, 0, v207, vcc
	v_fmac_f32_e32 v207, v205, v206
	s_waitcnt vmcnt(22)
	v_cmp_lt_i32_e32 vcc, 11, v54
	s_nop 1
	v_cndmask_b32_e32 v208, 1.0, v208, vcc
	v_cndmask_b32_e32 v209, 0, v209, vcc
	v_fmac_f32_e32 v209, v207, v208
	s_waitcnt vmcnt(21)
	v_cmp_lt_i32_e32 vcc, 12, v54
	s_nop 1
	v_cndmask_b32_e32 v210, 1.0, v210, vcc
	v_cndmask_b32_e32 v211, 0, v211, vcc
	v_fmac_f32_e32 v211, v209, v210
	s_waitcnt vmcnt(20)
	v_cmp_lt_i32_e32 vcc, 13, v54
	s_nop 1
	v_cndmask_b32_e32 v212, 1.0, v212, vcc
	v_cndmask_b32_e32 v213, 0, v213, vcc
	v_fmac_f32_e32 v213, v211, v212
	s_waitcnt vmcnt(19)
	v_cmp_lt_i32_e32 vcc, 14, v54
	s_nop 1
	v_cndmask_b32_e32 v214, 1.0, v214, vcc
	v_cndmask_b32_e32 v215, 0, v215, vcc
	v_fmac_f32_e32 v215, v213, v214
	s_waitcnt vmcnt(18)
	v_cmp_lt_i32_e32 vcc, 15, v54
	s_nop 1
	v_cndmask_b32_e32 v216, 1.0, v216, vcc
	v_cndmask_b32_e32 v217, 0, v217, vcc
	v_fmac_f32_e32 v217, v215, v216
	s_waitcnt vmcnt(17)
	v_cmp_lt_i32_e32 vcc, 16, v54
	s_nop 1
	v_cndmask_b32_e32 v218, 1.0, v218, vcc
	v_cndmask_b32_e32 v219, 0, v219, vcc
	v_fmac_f32_e32 v219, v217, v218
	s_waitcnt vmcnt(16)
	v_cmp_lt_i32_e32 vcc, 17, v54
	s_nop 1
	v_cndmask_b32_e32 v220, 1.0, v220, vcc
	v_cndmask_b32_e32 v221, 0, v221, vcc
	v_fmac_f32_e32 v221, v219, v220
	s_waitcnt vmcnt(15)
	v_cmp_lt_i32_e32 vcc, 18, v54
	s_nop 1
	v_cndmask_b32_e32 v222, 1.0, v222, vcc
	v_cndmask_b32_e32 v223, 0, v223, vcc
	v_fmac_f32_e32 v223, v221, v222
	s_waitcnt vmcnt(14)
	v_cmp_lt_i32_e32 vcc, 19, v54
	s_nop 1
	v_cndmask_b32_e32 v224, 1.0, v224, vcc
	v_cndmask_b32_e32 v225, 0, v225, vcc
	v_fmac_f32_e32 v225, v223, v224
	s_waitcnt vmcnt(13)
	v_cmp_lt_i32_e32 vcc, 20, v54
	s_nop 1
	v_cndmask_b32_e32 v226, 1.0, v226, vcc
	v_cndmask_b32_e32 v227, 0, v227, vcc
	v_fmac_f32_e32 v227, v225, v226
	s_waitcnt vmcnt(12)
	v_cmp_lt_i32_e32 vcc, 21, v54
	s_nop 1
	v_cndmask_b32_e32 v228, 1.0, v228, vcc
	v_cndmask_b32_e32 v229, 0, v229, vcc
	v_fmac_f32_e32 v229, v227, v228
	s_waitcnt vmcnt(11)
	v_cmp_lt_i32_e32 vcc, 22, v54
	s_nop 1
	v_cndmask_b32_e32 v230, 1.0, v230, vcc
	v_cndmask_b32_e32 v231, 0, v231, vcc
	v_fmac_f32_e32 v231, v229, v230
	s_waitcnt vmcnt(10)
	v_cmp_lt_i32_e32 vcc, 23, v54
	s_nop 1
	v_cndmask_b32_e32 v232, 1.0, v232, vcc
	v_cndmask_b32_e32 v233, 0, v233, vcc
	v_fmac_f32_e32 v233, v231, v232
	s_waitcnt vmcnt(9)
	v_cmp_lt_i32_e32 vcc, 24, v54
	s_nop 1
	v_cndmask_b32_e32 v234, 1.0, v234, vcc
	v_cndmask_b32_e32 v235, 0, v235, vcc
	v_fmac_f32_e32 v235, v233, v234
	s_waitcnt vmcnt(8)
	v_cmp_lt_i32_e32 vcc, 25, v54
	s_nop 1
	v_cndmask_b32_e32 v236, 1.0, v236, vcc
	v_cndmask_b32_e32 v237, 0, v237, vcc
	v_fmac_f32_e32 v237, v235, v236
	s_waitcnt vmcnt(7)
	v_cmp_lt_i32_e32 vcc, 26, v54
	s_nop 1
	v_cndmask_b32_e32 v238, 1.0, v238, vcc
	v_cndmask_b32_e32 v239, 0, v239, vcc
	v_fmac_f32_e32 v239, v237, v238
	s_waitcnt vmcnt(6)
	v_cmp_lt_i32_e32 vcc, 27, v54
	s_nop 1
	v_cndmask_b32_e32 v240, 1.0, v240, vcc
	v_cndmask_b32_e32 v241, 0, v241, vcc
	v_fmac_f32_e32 v241, v239, v240
	s_waitcnt vmcnt(5)
	v_cmp_lt_i32_e32 vcc, 28, v54
	s_nop 1
	v_cndmask_b32_e32 v242, 1.0, v242, vcc
	v_cndmask_b32_e32 v243, 0, v243, vcc
	v_fmac_f32_e32 v243, v241, v242
	s_waitcnt vmcnt(4)
	v_cmp_lt_i32_e32 vcc, 29, v54
	s_nop 1
	v_cndmask_b32_e32 v244, 1.0, v244, vcc
	v_cndmask_b32_e32 v245, 0, v245, vcc
	v_fmac_f32_e32 v245, v243, v244
	s_waitcnt vmcnt(3)
	v_cmp_lt_i32_e32 vcc, 30, v54
	s_nop 1
	v_cndmask_b32_e32 v246, 1.0, v246, vcc
	v_cndmask_b32_e32 v247, 0, v247, vcc
	v_fmac_f32_e32 v247, v245, v246
	s_waitcnt vmcnt(2)
	v_cmp_lt_i32_e32 vcc, 31, v54
	s_nop 1
	v_cndmask_b32_e32 v248, 1.0, v248, vcc
	v_cndmask_b32_e32 v249, 0, v249, vcc
	v_fmac_f32_e32 v249, v247, v248
	s_waitcnt vmcnt(1)
	v_cmp_lt_i32_e32 vcc, 32, v54
	s_nop 1
	v_cndmask_b32_e32 v250, 1.0, v250, vcc
	v_cndmask_b32_e32 v251, 0, v251, vcc
	v_fmac_f32_e32 v251, v249, v250
	s_waitcnt vmcnt(0)
	v_cmp_lt_i32_e32 vcc, 33, v54
	s_nop 1
	v_cndmask_b32_e32 v252, 1.0, v252, vcc
	v_cndmask_b32_e32 v253, 0, v253, vcc
	v_fmac_f32_e32 v253, v251, v252
	v_mov_b32_e32 v55, v253
	ds_write_b32 v183, v55 offset:59392
